# agg1: block csr window staged in LDS while the degree sort runs (one fewer dependent global round trip at start-up)
# baseline (speedup 1.0000x reference)
_Z11agg1_kernelPKDF16_PKfS2_PKiS4_S2_S2_PDF16_PfS6_i:
	s_load_dwordx8 s[4:11], s[0:1], 0x0
	s_load_dwordx8 s[12:19], s[0:1], 0x20
	s_load_dwordx4 s[20:23], s[0:1], 0x40
	s_load_dword s24, s[0:1], 0x50
	v_lshlrev_b32_e32 v32, 2, v0
	v_readfirstlane_b32 s25, v0
	s_lshl_b32 s26, s2, 5
	v_and_b32_e32 v64, 7, v0
	v_bfe_u32 v65, v0, 3, 3
	v_and_b32_e32 v45, 31, v0
	s_lshr_b32 s25, s25, 6
	v_lshlrev_b32_e32 v1, 1, v64
	v_add_u32_e32 v46, s26, v45
	s_waitcnt lgkmcnt(0)
	global_load_dword v33, v32, s[14:15]
	global_load_dword v34, v32, s[16:17]
	s_add_i32 s28, s24, -1
	v_cmp_gt_i32_e64 s[38:39], s24, v46
	v_min_i32_e32 v46, s28, v46
	v_lshlrev_b32_e32 v47, 2, v46
	global_load_dword v44, v47, s[10:11]
	global_load_dword v48, v47, s[10:11] offset:4
	s_lshl_b32 s27, s25, 11
	v_lshlrev_b32_e32 v62, 6, v64
	v_add_u32_e32 v62, 0x2000, v62
	v_cmp_eq_u32_e64 s[34:35], 0, v64
	v_lshlrev_b32_e32 v35, 8, v64
	v_lshl_add_u32 v35, v65, 4, v35
	v_add_u32_e32 v63, s27, v35
	v_mov_b32_e32 v36, 0
	v_mov_b32_e32 v37, 0
	v_mov_b32_e32 v38, 0
	v_mov_b32_e32 v39, 0
	s_waitcnt vmcnt(2)
	ds_write2st64_b32 v32, v33, v34 offset0:32 offset1:36
	ds_write_b128 v63, v[36:39]
	ds_write_b128 v63, v[36:39] offset:128
	s_waitcnt vmcnt(0)
	v_sub_u32_e32 v48, v48, v44
	v_add_u32_e32 v48, 1, v48
	v_cndmask_b32_e64 v48, 0, v48, s[38:39]
	v_lshl_or_b32 v40, v48, 5, v45
	v_readfirstlane_b32 s46, v44
	v_and_b32_e32 v49, 63, v0
	s_lshl_b32 s40, s25, 8
	v_add_u32_e32 v49, s40, v49
	v_add_u32_e32 v50, s46, v49
	v_lshlrev_b32_e32 v49, 2, v49
	v_min_u32_e32 v51, 0xc34ff, v50
	v_lshlrev_b32_e32 v51, 2, v51
	global_load_dword v52, v51, s[12:13]
	v_add_u32_e32 v51, 64, v50
	v_min_u32_e32 v51, 0xc34ff, v51
	v_lshlrev_b32_e32 v51, 2, v51
	global_load_dword v53, v51, s[12:13]
	v_add_u32_e32 v51, 0x80, v50
	v_min_u32_e32 v51, 0xc34ff, v51
	v_lshlrev_b32_e32 v51, 2, v51
	global_load_dword v54, v51, s[12:13]
	v_add_u32_e32 v51, 0xc0, v50
	v_min_u32_e32 v51, 0xc34ff, v51
	v_lshlrev_b32_e32 v51, 2, v51
	global_load_dword v55, v51, s[12:13]
	s_nop 1
	v_mov_b32_dpp v41, v40 quad_perm:[1,0,3,2] row_mask:0xf bank_mask:0xf
	s_mov_b32 s40, 0x99999999
	s_mov_b32 s41, 0x99999999
	v_min_u32_e32 v42, v40, v41
	v_max_u32_e32 v43, v40, v41
	v_cndmask_b32_e64 v40, v42, v43, s[40:41]
	s_nop 1
	v_mov_b32_dpp v41, v40 quad_perm:[2,3,0,1] row_mask:0xf bank_mask:0xf
	s_mov_b32 s40, 0xc3c3c3c3
	s_mov_b32 s41, 0xc3c3c3c3
	v_min_u32_e32 v42, v40, v41
	v_max_u32_e32 v43, v40, v41
	v_cndmask_b32_e64 v40, v42, v43, s[40:41]
	s_nop 1
	v_mov_b32_dpp v41, v40 quad_perm:[1,0,3,2] row_mask:0xf bank_mask:0xf
	s_mov_b32 s40, 0xa5a5a5a5
	s_mov_b32 s41, 0xa5a5a5a5
	v_min_u32_e32 v42, v40, v41
	v_max_u32_e32 v43, v40, v41
	v_cndmask_b32_e64 v40, v42, v43, s[40:41]
	ds_swizzle_b32 v41, v40 offset:swizzle(SWAP,4)
	s_waitcnt lgkmcnt(0)
	s_mov_b32 s40, 0xf00ff00f
	s_mov_b32 s41, 0xf00ff00f
	v_min_u32_e32 v42, v40, v41
	v_max_u32_e32 v43, v40, v41
	v_cndmask_b32_e64 v40, v42, v43, s[40:41]
	s_nop 1
	v_mov_b32_dpp v41, v40 quad_perm:[2,3,0,1] row_mask:0xf bank_mask:0xf
	s_mov_b32 s40, 0xcc33cc33
	s_mov_b32 s41, 0xcc33cc33
	v_min_u32_e32 v42, v40, v41
	v_max_u32_e32 v43, v40, v41
	v_cndmask_b32_e64 v40, v42, v43, s[40:41]
	s_nop 1
	v_mov_b32_dpp v41, v40 quad_perm:[1,0,3,2] row_mask:0xf bank_mask:0xf
	s_mov_b32 s40, 0xaa55aa55
	s_mov_b32 s41, 0xaa55aa55
	v_min_u32_e32 v42, v40, v41
	v_max_u32_e32 v43, v40, v41
	v_cndmask_b32_e64 v40, v42, v43, s[40:41]
	ds_swizzle_b32 v41, v40 offset:swizzle(SWAP,8)
	s_waitcnt lgkmcnt(0)
	s_mov_b32 s40, 0xff0000ff
	s_mov_b32 s41, 0xff0000ff
	v_min_u32_e32 v42, v40, v41
	v_max_u32_e32 v43, v40, v41
	v_cndmask_b32_e64 v40, v42, v43, s[40:41]
	ds_swizzle_b32 v41, v40 offset:swizzle(SWAP,4)
	s_waitcnt lgkmcnt(0)
	s_mov_b32 s40, 0xf0f00f0f
	s_mov_b32 s41, 0xf0f00f0f
	v_min_u32_e32 v42, v40, v41
	v_max_u32_e32 v43, v40, v41
	v_cndmask_b32_e64 v40, v42, v43, s[40:41]
	s_nop 1
	v_mov_b32_dpp v41, v40 quad_perm:[2,3,0,1] row_mask:0xf bank_mask:0xf
	s_mov_b32 s40, 0xcccc3333
	s_mov_b32 s41, 0xcccc3333
	v_min_u32_e32 v42, v40, v41
	v_max_u32_e32 v43, v40, v41
	v_cndmask_b32_e64 v40, v42, v43, s[40:41]
	s_nop 1
	v_mov_b32_dpp v41, v40 quad_perm:[1,0,3,2] row_mask:0xf bank_mask:0xf
	s_mov_b32 s40, 0xaaaa5555
	s_mov_b32 s41, 0xaaaa5555
	v_min_u32_e32 v42, v40, v41
	v_max_u32_e32 v43, v40, v41
	v_cndmask_b32_e64 v40, v42, v43, s[40:41]
	ds_swizzle_b32 v41, v40 offset:swizzle(SWAP,16)
	s_waitcnt lgkmcnt(0)
	s_mov_b32 s40, 0xffff
	s_mov_b32 s41, 0xffff
	v_min_u32_e32 v42, v40, v41
	v_max_u32_e32 v43, v40, v41
	v_cndmask_b32_e64 v40, v42, v43, s[40:41]
	ds_swizzle_b32 v41, v40 offset:swizzle(SWAP,8)
	s_waitcnt lgkmcnt(0)
	s_mov_b32 s40, 0xff00ff
	s_mov_b32 s41, 0xff00ff
	v_min_u32_e32 v42, v40, v41
	v_max_u32_e32 v43, v40, v41
	v_cndmask_b32_e64 v40, v42, v43, s[40:41]
	ds_swizzle_b32 v41, v40 offset:swizzle(SWAP,4)
	s_waitcnt lgkmcnt(0)
	s_mov_b32 s40, 0xf0f0f0f
	s_mov_b32 s41, 0xf0f0f0f
	v_min_u32_e32 v42, v40, v41
	v_max_u32_e32 v43, v40, v41
	v_cndmask_b32_e64 v40, v42, v43, s[40:41]
	s_nop 1
	v_mov_b32_dpp v41, v40 quad_perm:[2,3,0,1] row_mask:0xf bank_mask:0xf
	s_mov_b32 s40, 0x33333333
	s_mov_b32 s41, 0x33333333
	v_min_u32_e32 v42, v40, v41
	v_max_u32_e32 v43, v40, v41
	v_cndmask_b32_e64 v40, v42, v43, s[40:41]
	s_nop 1
	v_mov_b32_dpp v41, v40 quad_perm:[1,0,3,2] row_mask:0xf bank_mask:0xf
	s_mov_b32 s40, 0x55555555
	s_mov_b32 s41, 0x55555555
	v_min_u32_e32 v42, v40, v41
	v_max_u32_e32 v43, v40, v41
	v_cndmask_b32_e64 v40, v42, v43, s[40:41]
	s_waitcnt vmcnt(0)
	ds_write_b32 v49, v52 offset:10256
	ds_write_b32 v49, v53 offset:10512
	ds_write_b32 v49, v54 offset:10768
	ds_write_b32 v49, v55 offset:11024
	s_lshl_b32 s40, s25, 3
	v_add_u32_e32 v45, s40, v65
	v_lshlrev_b32_e32 v45, 2, v45
	ds_bpermute_b32 v46, v45, v40
	s_waitcnt lgkmcnt(0)
	v_and_b32_e32 v15, 31, v46
	v_lshrrev_b32_e32 v11, 5, v46
	v_lshlrev_b32_e32 v47, 2, v15
	ds_bpermute_b32 v10, v47, v44
	v_add_u32_e32 v66, s26, v15
	v_min_i32_e32 v66, s28, v66
	v_cmp_lt_u32_e64 s[36:37], 0, v11
	v_lshlrev_b32_e32 v4, 2, v66
	v_lshlrev_b32_e32 v35, 2, v64
	v_lshl_or_b32 v35, v66, 5, v35
	global_load_dword v9, v35, s[8:9]
	v_lshrrev_b32_e32 v3, 3, v15
	v_lshlrev_b32_e32 v3, 11, v3
	v_and_b32_e32 v47, 7, v15
	v_lshl_add_u32 v3, v47, 1, v3
	v_lshl_add_u32 v3, v64, 4, v3
	v_readfirstlane_b32 s29, v11
	s_waitcnt lgkmcnt(0)
	s_barrier
	v_subrev_u32_e32 v67, s46, v10
	v_add_u32_e32 v67, v67, v64
	v_add_u32_e32 v67, -1, v67
	v_mov_b32_e32 v5, s24
	v_mov_b32_e32 v6, s24
	v_mov_b32_e32 v7, s24
	v_mov_b32_e32 v8, s24
	v_cndmask_b32_e64 v5, v5, v66, s[34:35]
	v_cmp_gt_i32_e32 vcc, v11, v64
	s_andn2_b64 s[40:41], vcc, s[34:35]
	v_cmp_gt_u32_e32 vcc, 0x400, v67
	s_and_b64 s[44:45], s[40:41], vcc
	s_andn2_b64 s[40:41], s[40:41], vcc
	s_and_saveexec_b64 s[32:33], s[44:45]
	v_lshlrev_b32_e32 v32, 2, v67
	ds_read_b32 v5, v32 offset:10256
	s_mov_b64 exec, s[32:33]
	s_and_saveexec_b64 s[32:33], s[40:41]
	v_add_lshl_u32 v32, v67, s46, 2
	global_load_dword v5, v32, s[12:13]
	s_mov_b64 exec, s[32:33]
	v_add_u32_e32 v68, 8, v64
	v_cmp_gt_i32_e64 s[40:41], v11, v68
	v_add_u32_e32 v67, 8, v67
	v_cmp_gt_u32_e32 vcc, 0x400, v67
	s_and_b64 s[44:45], s[40:41], vcc
	s_andn2_b64 s[40:41], s[40:41], vcc
	s_and_saveexec_b64 s[32:33], s[44:45]
	v_lshlrev_b32_e32 v33, 2, v67
	ds_read_b32 v6, v33 offset:10256
	s_mov_b64 exec, s[32:33]
	s_and_saveexec_b64 s[32:33], s[40:41]
	v_add_lshl_u32 v33, v67, s46, 2
	global_load_dword v6, v33, s[12:13]
	s_mov_b64 exec, s[32:33]
	v_add_u32_e32 v68, 16, v64
	v_cmp_gt_i32_e64 s[40:41], v11, v68
	v_add_u32_e32 v67, 8, v67
	v_cmp_gt_u32_e32 vcc, 0x400, v67
	s_and_b64 s[44:45], s[40:41], vcc
	s_andn2_b64 s[40:41], s[40:41], vcc
	s_and_saveexec_b64 s[32:33], s[44:45]
	v_lshlrev_b32_e32 v34, 2, v67
	ds_read_b32 v7, v34 offset:10256
	s_mov_b64 exec, s[32:33]
	s_and_saveexec_b64 s[32:33], s[40:41]
	v_add_lshl_u32 v34, v67, s46, 2
	global_load_dword v7, v34, s[12:13]
	s_mov_b64 exec, s[32:33]
	v_add_u32_e32 v68, 24, v64
	v_cmp_gt_i32_e64 s[40:41], v11, v68
	v_add_u32_e32 v67, 8, v67
	v_cmp_gt_u32_e32 vcc, 0x400, v67
	s_and_b64 s[44:45], s[40:41], vcc
	s_andn2_b64 s[40:41], s[40:41], vcc
	s_and_saveexec_b64 s[32:33], s[44:45]
	v_lshlrev_b32_e32 v35, 2, v67
	ds_read_b32 v8, v35 offset:10256
	s_mov_b64 exec, s[32:33]
	s_and_saveexec_b64 s[32:33], s[40:41]
	v_add_lshl_u32 v35, v67, s46, 2
	global_load_dword v8, v35, s[12:13]
	s_mov_b64 exec, s[32:33]
	s_waitcnt vmcnt(0) lgkmcnt(0)
	v_lshlrev_b32_e32 v5, 4, v5
	v_lshlrev_b32_e32 v6, 4, v6
	v_lshlrev_b32_e32 v7, 4, v7
	v_lshlrev_b32_e32 v8, 4, v8
	s_mov_b32 s42, 0
	s_mov_b32 s43, 0
	s_cmp_lt_i32 s29, 3
	s_cbranch_scc1 .Lagg_first_half
	ds_swizzle_b32 v32, v5 offset:swizzle(BITMASK_PERM, "pp000")
	ds_swizzle_b32 v33, v5 offset:swizzle(BITMASK_PERM, "pp001")
	ds_swizzle_b32 v34, v5 offset:swizzle(BITMASK_PERM, "pp010")
	ds_swizzle_b32 v35, v5 offset:swizzle(BITMASK_PERM, "pp011")
	s_waitcnt lgkmcnt(0)
	v_or_b32_e32 v32, v32, v1
	v_or_b32_e32 v33, v33, v1
	v_or_b32_e32 v34, v34, v1
	v_or_b32_e32 v35, v35, v1
	global_load_ushort v36, v32, s[6:7]
	global_load_ushort v37, v33, s[6:7]
	global_load_ushort v38, v34, s[6:7]
	global_load_ushort v39, v35, s[6:7]
	v_lshlrev_b32_e32 v32, 3, v32
	v_lshlrev_b32_e32 v33, 3, v33
	v_lshlrev_b32_e32 v34, 3, v34
	v_lshlrev_b32_e32 v35, 3, v35
	global_load_dwordx4 v[40:43], v32, s[4:5]
	global_load_dwordx4 v[44:47], v33, s[4:5]
	global_load_dwordx4 v[48:51], v34, s[4:5]
	global_load_dwordx4 v[52:55], v35, s[4:5]
	s_waitcnt vmcnt(4)
	v_fma_mix_f32 v36, v36, 1.0, v9 op_sel_hi:[1,0,0]
	v_fma_mix_f32 v37, v37, 1.0, v9 op_sel_hi:[1,0,0]
	v_fma_mix_f32 v38, v38, 1.0, v9 op_sel_hi:[1,0,0]
	v_fma_mix_f32 v39, v39, 1.0, v9 op_sel_hi:[1,0,0]
	v_mul_f32_e32 v58, 0x3e4ccccd, v36
	v_mul_f32_e32 v59, 0x3e4ccccd, v37
	v_mul_f32_e32 v60, 0x3e4ccccd, v38
	v_mul_f32_e32 v61, 0x3e4ccccd, v39
	v_max_f32_e32 v36, v36, v58
	v_max_f32_e32 v37, v37, v59
	v_max_f32_e32 v38, v38, v60
	v_max_f32_e32 v39, v39, v61
	v_max3_f32 v56, v36, v37, v38
	v_max_f32_e32 v13, v56, v39
	v_sub_f32_e32 v36, v36, v13
	v_sub_f32_e32 v37, v37, v13
	v_sub_f32_e32 v38, v38, v13
	v_sub_f32_e32 v39, v39, v13
	v_exp_f32_e32 v36, v36
	v_exp_f32_e32 v37, v37
	v_exp_f32_e32 v38, v38
	v_exp_f32_e32 v39, v39
	s_nop 0
	v_add_f32_e32 v14, v36, v37
	v_add_f32_e32 v14, v14, v38
	v_add_f32_e32 v14, v14, v39
	s_waitcnt vmcnt(3)
	v_cvt_scalef32_pk_f16_fp8 v58, v40, 1.0
	v_cvt_scalef32_pk_f16_fp8 v59, v40, 1.0 op_sel:[1,0,0]
	v_cvt_scalef32_pk_f16_fp8 v60, v41, 1.0
	v_cvt_scalef32_pk_f16_fp8 v61, v41, 1.0 op_sel:[1,0,0]
	v_fma_mix_f32 v16, v58, v36, 0 op_sel_hi:[1,0,0]
	v_fma_mix_f32 v17, v58, v36, 0 op_sel:[1,0,0] op_sel_hi:[1,0,0]
	v_fma_mix_f32 v18, v59, v36, 0 op_sel_hi:[1,0,0]
	v_fma_mix_f32 v19, v59, v36, 0 op_sel:[1,0,0] op_sel_hi:[1,0,0]
	v_fma_mix_f32 v20, v60, v36, 0 op_sel_hi:[1,0,0]
	v_fma_mix_f32 v21, v60, v36, 0 op_sel:[1,0,0] op_sel_hi:[1,0,0]
	v_fma_mix_f32 v22, v61, v36, 0 op_sel_hi:[1,0,0]
	v_fma_mix_f32 v23, v61, v36, 0 op_sel:[1,0,0] op_sel_hi:[1,0,0]
	v_cvt_scalef32_pk_f16_fp8 v58, v42, 1.0
	v_cvt_scalef32_pk_f16_fp8 v59, v42, 1.0 op_sel:[1,0,0]
	v_cvt_scalef32_pk_f16_fp8 v60, v43, 1.0
	v_cvt_scalef32_pk_f16_fp8 v61, v43, 1.0 op_sel:[1,0,0]
	v_fma_mix_f32 v24, v58, v36, 0 op_sel_hi:[1,0,0]
	v_fma_mix_f32 v25, v58, v36, 0 op_sel:[1,0,0] op_sel_hi:[1,0,0]
	v_fma_mix_f32 v26, v59, v36, 0 op_sel_hi:[1,0,0]
	v_fma_mix_f32 v27, v59, v36, 0 op_sel:[1,0,0] op_sel_hi:[1,0,0]
	v_fma_mix_f32 v28, v60, v36, 0 op_sel_hi:[1,0,0]
	v_fma_mix_f32 v29, v60, v36, 0 op_sel:[1,0,0] op_sel_hi:[1,0,0]
	v_fma_mix_f32 v30, v61, v36, 0 op_sel_hi:[1,0,0]
	v_fma_mix_f32 v31, v61, v36, 0 op_sel:[1,0,0] op_sel_hi:[1,0,0]
	s_waitcnt vmcnt(2)
	v_cvt_scalef32_pk_f16_fp8 v58, v44, 1.0
	v_cvt_scalef32_pk_f16_fp8 v59, v44, 1.0 op_sel:[1,0,0]
	v_cvt_scalef32_pk_f16_fp8 v60, v45, 1.0
	v_cvt_scalef32_pk_f16_fp8 v61, v45, 1.0 op_sel:[1,0,0]
	v_fma_mix_f32 v16, v58, v37, v16 op_sel_hi:[1,0,0]
	v_fma_mix_f32 v17, v58, v37, v17 op_sel:[1,0,0] op_sel_hi:[1,0,0]
	v_fma_mix_f32 v18, v59, v37, v18 op_sel_hi:[1,0,0]
	v_fma_mix_f32 v19, v59, v37, v19 op_sel:[1,0,0] op_sel_hi:[1,0,0]
	v_fma_mix_f32 v20, v60, v37, v20 op_sel_hi:[1,0,0]
	v_fma_mix_f32 v21, v60, v37, v21 op_sel:[1,0,0] op_sel_hi:[1,0,0]
	v_fma_mix_f32 v22, v61, v37, v22 op_sel_hi:[1,0,0]
	v_fma_mix_f32 v23, v61, v37, v23 op_sel:[1,0,0] op_sel_hi:[1,0,0]
	v_cvt_scalef32_pk_f16_fp8 v58, v46, 1.0
	v_cvt_scalef32_pk_f16_fp8 v59, v46, 1.0 op_sel:[1,0,0]
	v_cvt_scalef32_pk_f16_fp8 v60, v47, 1.0
	v_cvt_scalef32_pk_f16_fp8 v61, v47, 1.0 op_sel:[1,0,0]
	v_fma_mix_f32 v24, v58, v37, v24 op_sel_hi:[1,0,0]
	v_fma_mix_f32 v25, v58, v37, v25 op_sel:[1,0,0] op_sel_hi:[1,0,0]
	v_fma_mix_f32 v26, v59, v37, v26 op_sel_hi:[1,0,0]
	v_fma_mix_f32 v27, v59, v37, v27 op_sel:[1,0,0] op_sel_hi:[1,0,0]
	v_fma_mix_f32 v28, v60, v37, v28 op_sel_hi:[1,0,0]
	v_fma_mix_f32 v29, v60, v37, v29 op_sel:[1,0,0] op_sel_hi:[1,0,0]
	v_fma_mix_f32 v30, v61, v37, v30 op_sel_hi:[1,0,0]
	v_fma_mix_f32 v31, v61, v37, v31 op_sel:[1,0,0] op_sel_hi:[1,0,0]
	s_waitcnt vmcnt(1)
	v_cvt_scalef32_pk_f16_fp8 v58, v48, 1.0
	v_cvt_scalef32_pk_f16_fp8 v59, v48, 1.0 op_sel:[1,0,0]
	v_cvt_scalef32_pk_f16_fp8 v60, v49, 1.0
	v_cvt_scalef32_pk_f16_fp8 v61, v49, 1.0 op_sel:[1,0,0]
	v_fma_mix_f32 v16, v58, v38, v16 op_sel_hi:[1,0,0]
	v_fma_mix_f32 v17, v58, v38, v17 op_sel:[1,0,0] op_sel_hi:[1,0,0]
	v_fma_mix_f32 v18, v59, v38, v18 op_sel_hi:[1,0,0]
	v_fma_mix_f32 v19, v59, v38, v19 op_sel:[1,0,0] op_sel_hi:[1,0,0]
	v_fma_mix_f32 v20, v60, v38, v20 op_sel_hi:[1,0,0]
	v_fma_mix_f32 v21, v60, v38, v21 op_sel:[1,0,0] op_sel_hi:[1,0,0]
	v_fma_mix_f32 v22, v61, v38, v22 op_sel_hi:[1,0,0]
	v_fma_mix_f32 v23, v61, v38, v23 op_sel:[1,0,0] op_sel_hi:[1,0,0]
	v_cvt_scalef32_pk_f16_fp8 v58, v50, 1.0
	v_cvt_scalef32_pk_f16_fp8 v59, v50, 1.0 op_sel:[1,0,0]
	v_cvt_scalef32_pk_f16_fp8 v60, v51, 1.0
	v_cvt_scalef32_pk_f16_fp8 v61, v51, 1.0 op_sel:[1,0,0]
	v_fma_mix_f32 v24, v58, v38, v24 op_sel_hi:[1,0,0]
	v_fma_mix_f32 v25, v58, v38, v25 op_sel:[1,0,0] op_sel_hi:[1,0,0]
	v_fma_mix_f32 v26, v59, v38, v26 op_sel_hi:[1,0,0]
	v_fma_mix_f32 v27, v59, v38, v27 op_sel:[1,0,0] op_sel_hi:[1,0,0]
	v_fma_mix_f32 v28, v60, v38, v28 op_sel_hi:[1,0,0]
	v_fma_mix_f32 v29, v60, v38, v29 op_sel:[1,0,0] op_sel_hi:[1,0,0]
	v_fma_mix_f32 v30, v61, v38, v30 op_sel_hi:[1,0,0]
	v_fma_mix_f32 v31, v61, v38, v31 op_sel:[1,0,0] op_sel_hi:[1,0,0]
	s_waitcnt vmcnt(0)
	v_cvt_scalef32_pk_f16_fp8 v58, v52, 1.0
	v_cvt_scalef32_pk_f16_fp8 v59, v52, 1.0 op_sel:[1,0,0]
	v_cvt_scalef32_pk_f16_fp8 v60, v53, 1.0
	v_cvt_scalef32_pk_f16_fp8 v61, v53, 1.0 op_sel:[1,0,0]
	v_fma_mix_f32 v16, v58, v39, v16 op_sel_hi:[1,0,0]
	v_fma_mix_f32 v17, v58, v39, v17 op_sel:[1,0,0] op_sel_hi:[1,0,0]
	v_fma_mix_f32 v18, v59, v39, v18 op_sel_hi:[1,0,0]
	v_fma_mix_f32 v19, v59, v39, v19 op_sel:[1,0,0] op_sel_hi:[1,0,0]
	v_fma_mix_f32 v20, v60, v39, v20 op_sel_hi:[1,0,0]
	v_fma_mix_f32 v21, v60, v39, v21 op_sel:[1,0,0] op_sel_hi:[1,0,0]
	v_fma_mix_f32 v22, v61, v39, v22 op_sel_hi:[1,0,0]
	v_fma_mix_f32 v23, v61, v39, v23 op_sel:[1,0,0] op_sel_hi:[1,0,0]
	v_cvt_scalef32_pk_f16_fp8 v58, v54, 1.0
	v_cvt_scalef32_pk_f16_fp8 v59, v54, 1.0 op_sel:[1,0,0]
	v_cvt_scalef32_pk_f16_fp8 v60, v55, 1.0
	v_cvt_scalef32_pk_f16_fp8 v61, v55, 1.0 op_sel:[1,0,0]
	v_fma_mix_f32 v24, v58, v39, v24 op_sel_hi:[1,0,0]
	v_fma_mix_f32 v25, v58, v39, v25 op_sel:[1,0,0] op_sel_hi:[1,0,0]
	v_fma_mix_f32 v26, v59, v39, v26 op_sel_hi:[1,0,0]
	v_fma_mix_f32 v27, v59, v39, v27 op_sel:[1,0,0] op_sel_hi:[1,0,0]
	v_fma_mix_f32 v28, v60, v39, v28 op_sel_hi:[1,0,0]
	v_fma_mix_f32 v29, v60, v39, v29 op_sel:[1,0,0] op_sel_hi:[1,0,0]
	v_fma_mix_f32 v30, v61, v39, v30 op_sel_hi:[1,0,0]
	v_fma_mix_f32 v31, v61, v39, v31 op_sel:[1,0,0] op_sel_hi:[1,0,0]
	s_sub_i32 s29, s29, 4
	s_branch .Lagg_B

.Lagg_B:
	s_cmp_lt_i32 s29, 1
	s_cbranch_scc1 .Lagg_epi
	s_cmp_lt_i32 s29, 3
	s_cbranch_scc1 .Lagg_B_half
	ds_swizzle_b32 v32, v5 offset:swizzle(BITMASK_PERM, "pp100")
	ds_swizzle_b32 v33, v5 offset:swizzle(BITMASK_PERM, "pp101")
	ds_swizzle_b32 v34, v5 offset:swizzle(BITMASK_PERM, "pp110")
	ds_swizzle_b32 v35, v5 offset:swizzle(BITMASK_PERM, "pp111")
	s_waitcnt lgkmcnt(0)
	v_or_b32_e32 v32, v32, v1
	v_or_b32_e32 v33, v33, v1
	v_or_b32_e32 v34, v34, v1
	v_or_b32_e32 v35, v35, v1
	global_load_ushort v36, v32, s[6:7]
	global_load_ushort v37, v33, s[6:7]
	global_load_ushort v38, v34, s[6:7]
	global_load_ushort v39, v35, s[6:7]
	v_lshlrev_b32_e32 v32, 3, v32
	v_lshlrev_b32_e32 v33, 3, v33
	v_lshlrev_b32_e32 v34, 3, v34
	v_lshlrev_b32_e32 v35, 3, v35
	global_load_dwordx4 v[40:43], v32, s[4:5]
	global_load_dwordx4 v[44:47], v33, s[4:5]
	global_load_dwordx4 v[48:51], v34, s[4:5]
	global_load_dwordx4 v[52:55], v35, s[4:5]
	s_waitcnt vmcnt(4)
	v_fma_mix_f32 v36, v36, 1.0, v9 op_sel_hi:[1,0,0]
	v_fma_mix_f32 v37, v37, 1.0, v9 op_sel_hi:[1,0,0]
	v_fma_mix_f32 v38, v38, 1.0, v9 op_sel_hi:[1,0,0]
	v_fma_mix_f32 v39, v39, 1.0, v9 op_sel_hi:[1,0,0]
	v_mul_f32_e32 v58, 0x3e4ccccd, v36
	v_mul_f32_e32 v59, 0x3e4ccccd, v37
	v_mul_f32_e32 v60, 0x3e4ccccd, v38
	v_mul_f32_e32 v61, 0x3e4ccccd, v39
	v_max_f32_e32 v36, v36, v58
	v_max_f32_e32 v37, v37, v59
	v_max_f32_e32 v38, v38, v60
	v_max_f32_e32 v39, v39, v61
	v_max3_f32 v56, v13, v36, v37
	v_max3_f32 v12, v56, v38, v39
	v_sub_f32_e32 v57, v13, v12
	v_sub_f32_e32 v36, v36, v12
	v_sub_f32_e32 v37, v37, v12
	v_sub_f32_e32 v38, v38, v12
	v_sub_f32_e32 v39, v39, v12
	v_exp_f32_e32 v57, v57
	v_exp_f32_e32 v36, v36
	v_exp_f32_e32 v37, v37
	v_exp_f32_e32 v38, v38
	v_exp_f32_e32 v39, v39
	v_fma_f32 v14, v14, v57, v36
	v_mul_f32_e32 v16, v16, v57
	v_mul_f32_e32 v17, v17, v57
	v_mul_f32_e32 v18, v18, v57
	v_mul_f32_e32 v19, v19, v57
	v_mul_f32_e32 v20, v20, v57
	v_mul_f32_e32 v21, v21, v57
	v_mul_f32_e32 v22, v22, v57
	v_mul_f32_e32 v23, v23, v57
	v_mul_f32_e32 v24, v24, v57
	v_mul_f32_e32 v25, v25, v57
	v_mul_f32_e32 v26, v26, v57
	v_mul_f32_e32 v27, v27, v57
	v_mul_f32_e32 v28, v28, v57
	v_mul_f32_e32 v29, v29, v57
	v_mul_f32_e32 v30, v30, v57
	v_mul_f32_e32 v31, v31, v57
	v_add_f32_e32 v14, v14, v37
	v_add_f32_e32 v14, v14, v38
	v_add_f32_e32 v14, v14, v39
	s_waitcnt vmcnt(3)
	v_cvt_scalef32_pk_f16_fp8 v58, v40, 1.0
	v_cvt_scalef32_pk_f16_fp8 v59, v40, 1.0 op_sel:[1,0,0]
	v_cvt_scalef32_pk_f16_fp8 v60, v41, 1.0
	v_cvt_scalef32_pk_f16_fp8 v61, v41, 1.0 op_sel:[1,0,0]
	v_fma_mix_f32 v16, v58, v36, v16 op_sel_hi:[1,0,0]
	v_fma_mix_f32 v17, v58, v36, v17 op_sel:[1,0,0] op_sel_hi:[1,0,0]
	v_fma_mix_f32 v18, v59, v36, v18 op_sel_hi:[1,0,0]
	v_fma_mix_f32 v19, v59, v36, v19 op_sel:[1,0,0] op_sel_hi:[1,0,0]
	v_fma_mix_f32 v20, v60, v36, v20 op_sel_hi:[1,0,0]
	v_fma_mix_f32 v21, v60, v36, v21 op_sel:[1,0,0] op_sel_hi:[1,0,0]
	v_fma_mix_f32 v22, v61, v36, v22 op_sel_hi:[1,0,0]
	v_fma_mix_f32 v23, v61, v36, v23 op_sel:[1,0,0] op_sel_hi:[1,0,0]
	v_cvt_scalef32_pk_f16_fp8 v58, v42, 1.0
	v_cvt_scalef32_pk_f16_fp8 v59, v42, 1.0 op_sel:[1,0,0]
	v_cvt_scalef32_pk_f16_fp8 v60, v43, 1.0
	v_cvt_scalef32_pk_f16_fp8 v61, v43, 1.0 op_sel:[1,0,0]
	v_fma_mix_f32 v24, v58, v36, v24 op_sel_hi:[1,0,0]
	v_fma_mix_f32 v25, v58, v36, v25 op_sel:[1,0,0] op_sel_hi:[1,0,0]
	v_fma_mix_f32 v26, v59, v36, v26 op_sel_hi:[1,0,0]
	v_fma_mix_f32 v27, v59, v36, v27 op_sel:[1,0,0] op_sel_hi:[1,0,0]
	v_fma_mix_f32 v28, v60, v36, v28 op_sel_hi:[1,0,0]
	v_fma_mix_f32 v29, v60, v36, v29 op_sel:[1,0,0] op_sel_hi:[1,0,0]
	v_fma_mix_f32 v30, v61, v36, v30 op_sel_hi:[1,0,0]
	v_fma_mix_f32 v31, v61, v36, v31 op_sel:[1,0,0] op_sel_hi:[1,0,0]
	s_waitcnt vmcnt(2)
	v_cvt_scalef32_pk_f16_fp8 v58, v44, 1.0
	v_cvt_scalef32_pk_f16_fp8 v59, v44, 1.0 op_sel:[1,0,0]
	v_cvt_scalef32_pk_f16_fp8 v60, v45, 1.0
	v_cvt_scalef32_pk_f16_fp8 v61, v45, 1.0 op_sel:[1,0,0]
	v_fma_mix_f32 v16, v58, v37, v16 op_sel_hi:[1,0,0]
	v_fma_mix_f32 v17, v58, v37, v17 op_sel:[1,0,0] op_sel_hi:[1,0,0]
	v_fma_mix_f32 v18, v59, v37, v18 op_sel_hi:[1,0,0]
	v_fma_mix_f32 v19, v59, v37, v19 op_sel:[1,0,0] op_sel_hi:[1,0,0]
	v_fma_mix_f32 v20, v60, v37, v20 op_sel_hi:[1,0,0]
	v_fma_mix_f32 v21, v60, v37, v21 op_sel:[1,0,0] op_sel_hi:[1,0,0]
	v_fma_mix_f32 v22, v61, v37, v22 op_sel_hi:[1,0,0]
	v_fma_mix_f32 v23, v61, v37, v23 op_sel:[1,0,0] op_sel_hi:[1,0,0]
	v_cvt_scalef32_pk_f16_fp8 v58, v46, 1.0
	v_cvt_scalef32_pk_f16_fp8 v59, v46, 1.0 op_sel:[1,0,0]
	v_cvt_scalef32_pk_f16_fp8 v60, v47, 1.0
	v_cvt_scalef32_pk_f16_fp8 v61, v47, 1.0 op_sel:[1,0,0]
	v_fma_mix_f32 v24, v58, v37, v24 op_sel_hi:[1,0,0]
	v_fma_mix_f32 v25, v58, v37, v25 op_sel:[1,0,0] op_sel_hi:[1,0,0]
	v_fma_mix_f32 v26, v59, v37, v26 op_sel_hi:[1,0,0]
	v_fma_mix_f32 v27, v59, v37, v27 op_sel:[1,0,0] op_sel_hi:[1,0,0]
	v_fma_mix_f32 v28, v60, v37, v28 op_sel_hi:[1,0,0]
	v_fma_mix_f32 v29, v60, v37, v29 op_sel:[1,0,0] op_sel_hi:[1,0,0]
	v_fma_mix_f32 v30, v61, v37, v30 op_sel_hi:[1,0,0]
	v_fma_mix_f32 v31, v61, v37, v31 op_sel:[1,0,0] op_sel_hi:[1,0,0]
	s_waitcnt vmcnt(1)
	v_cvt_scalef32_pk_f16_fp8 v58, v48, 1.0
	v_cvt_scalef32_pk_f16_fp8 v59, v48, 1.0 op_sel:[1,0,0]
	v_cvt_scalef32_pk_f16_fp8 v60, v49, 1.0
	v_cvt_scalef32_pk_f16_fp8 v61, v49, 1.0 op_sel:[1,0,0]
	v_fma_mix_f32 v16, v58, v38, v16 op_sel_hi:[1,0,0]
	v_fma_mix_f32 v17, v58, v38, v17 op_sel:[1,0,0] op_sel_hi:[1,0,0]
	v_fma_mix_f32 v18, v59, v38, v18 op_sel_hi:[1,0,0]
	v_fma_mix_f32 v19, v59, v38, v19 op_sel:[1,0,0] op_sel_hi:[1,0,0]
	v_fma_mix_f32 v20, v60, v38, v20 op_sel_hi:[1,0,0]
	v_fma_mix_f32 v21, v60, v38, v21 op_sel:[1,0,0] op_sel_hi:[1,0,0]
	v_fma_mix_f32 v22, v61, v38, v22 op_sel_hi:[1,0,0]
	v_fma_mix_f32 v23, v61, v38, v23 op_sel:[1,0,0] op_sel_hi:[1,0,0]
	v_cvt_scalef32_pk_f16_fp8 v58, v50, 1.0
	v_cvt_scalef32_pk_f16_fp8 v59, v50, 1.0 op_sel:[1,0,0]
	v_cvt_scalef32_pk_f16_fp8 v60, v51, 1.0
	v_cvt_scalef32_pk_f16_fp8 v61, v51, 1.0 op_sel:[1,0,0]
	v_fma_mix_f32 v24, v58, v38, v24 op_sel_hi:[1,0,0]
	v_fma_mix_f32 v25, v58, v38, v25 op_sel:[1,0,0] op_sel_hi:[1,0,0]
	v_fma_mix_f32 v26, v59, v38, v26 op_sel_hi:[1,0,0]
	v_fma_mix_f32 v27, v59, v38, v27 op_sel:[1,0,0] op_sel_hi:[1,0,0]
	v_fma_mix_f32 v28, v60, v38, v28 op_sel_hi:[1,0,0]
	v_fma_mix_f32 v29, v60, v38, v29 op_sel:[1,0,0] op_sel_hi:[1,0,0]
	v_fma_mix_f32 v30, v61, v38, v30 op_sel_hi:[1,0,0]
	v_fma_mix_f32 v31, v61, v38, v31 op_sel:[1,0,0] op_sel_hi:[1,0,0]
	s_waitcnt vmcnt(0)
	v_cvt_scalef32_pk_f16_fp8 v58, v52, 1.0
	v_cvt_scalef32_pk_f16_fp8 v59, v52, 1.0 op_sel:[1,0,0]
	v_cvt_scalef32_pk_f16_fp8 v60, v53, 1.0
	v_cvt_scalef32_pk_f16_fp8 v61, v53, 1.0 op_sel:[1,0,0]
	v_fma_mix_f32 v16, v58, v39, v16 op_sel_hi:[1,0,0]
	v_fma_mix_f32 v17, v58, v39, v17 op_sel:[1,0,0] op_sel_hi:[1,0,0]
	v_fma_mix_f32 v18, v59, v39, v18 op_sel_hi:[1,0,0]
	v_fma_mix_f32 v19, v59, v39, v19 op_sel:[1,0,0] op_sel_hi:[1,0,0]
	v_fma_mix_f32 v20, v60, v39, v20 op_sel_hi:[1,0,0]
	v_fma_mix_f32 v21, v60, v39, v21 op_sel:[1,0,0] op_sel_hi:[1,0,0]
	v_fma_mix_f32 v22, v61, v39, v22 op_sel_hi:[1,0,0]
	v_fma_mix_f32 v23, v61, v39, v23 op_sel:[1,0,0] op_sel_hi:[1,0,0]
	v_cvt_scalef32_pk_f16_fp8 v58, v54, 1.0
	v_cvt_scalef32_pk_f16_fp8 v59, v54, 1.0 op_sel:[1,0,0]
	v_cvt_scalef32_pk_f16_fp8 v60, v55, 1.0
	v_cvt_scalef32_pk_f16_fp8 v61, v55, 1.0 op_sel:[1,0,0]
	v_fma_mix_f32 v24, v58, v39, v24 op_sel_hi:[1,0,0]
	v_fma_mix_f32 v25, v58, v39, v25 op_sel:[1,0,0] op_sel_hi:[1,0,0]
	v_fma_mix_f32 v26, v59, v39, v26 op_sel_hi:[1,0,0]
	v_fma_mix_f32 v27, v59, v39, v27 op_sel:[1,0,0] op_sel_hi:[1,0,0]
	v_fma_mix_f32 v28, v60, v39, v28 op_sel_hi:[1,0,0]
	v_fma_mix_f32 v29, v60, v39, v29 op_sel:[1,0,0] op_sel_hi:[1,0,0]
	v_fma_mix_f32 v30, v61, v39, v30 op_sel_hi:[1,0,0]
	v_fma_mix_f32 v31, v61, v39, v31 op_sel:[1,0,0] op_sel_hi:[1,0,0]
	s_sub_i32 s29, s29, 4
	v_mov_b32_e32 v5, v6
	v_mov_b32_e32 v6, v7
	v_mov_b32_e32 v7, v8
	s_add_i32 s43, s43, 1
	s_cmp_lt_i32 s29, 1
	s_cbranch_scc1 .Lagg_epi
	s_cmp_lg_u32 s43, 4
	s_cbranch_scc1 .Lagg_A
	s_add_i32 s42, s42, 32
	s_mov_b32 s43, 0
	v_subrev_u32_e32 v67, s46, v10
	v_add_u32_e32 v67, v67, v64
	v_add_u32_e32 v67, s42, v67
	v_add_u32_e32 v68, s42, v64
	v_add_u32_e32 v67, -1, v67
	v_mov_b32_e32 v5, s24
	v_mov_b32_e32 v6, s24
	v_mov_b32_e32 v7, s24
	v_mov_b32_e32 v8, s24
	v_cmp_gt_i32_e64 s[40:41], v11, v68
	v_cmp_gt_u32_e32 vcc, 0x400, v67
	s_and_b64 s[44:45], s[40:41], vcc
	s_andn2_b64 s[40:41], s[40:41], vcc
	s_and_saveexec_b64 s[32:33], s[44:45]
	v_lshlrev_b32_e32 v32, 2, v67
	ds_read_b32 v5, v32 offset:10256
	s_mov_b64 exec, s[32:33]
	s_and_saveexec_b64 s[32:33], s[40:41]
	v_add_lshl_u32 v32, v67, s46, 2
	global_load_dword v5, v32, s[12:13]
	s_mov_b64 exec, s[32:33]
	v_add_u32_e32 v68, 8, v68
	v_cmp_gt_i32_e64 s[40:41], v11, v68
	v_add_u32_e32 v67, 8, v67
	v_cmp_gt_u32_e32 vcc, 0x400, v67
	s_and_b64 s[44:45], s[40:41], vcc
	s_andn2_b64 s[40:41], s[40:41], vcc
	s_and_saveexec_b64 s[32:33], s[44:45]
	v_lshlrev_b32_e32 v33, 2, v67
	ds_read_b32 v6, v33 offset:10256
	s_mov_b64 exec, s[32:33]
	s_and_saveexec_b64 s[32:33], s[40:41]
	v_add_lshl_u32 v33, v67, s46, 2
	global_load_dword v6, v33, s[12:13]
	s_mov_b64 exec, s[32:33]
	v_add_u32_e32 v68, 8, v68
	v_cmp_gt_i32_e64 s[40:41], v11, v68
	v_add_u32_e32 v67, 8, v67
	v_cmp_gt_u32_e32 vcc, 0x400, v67
	s_and_b64 s[44:45], s[40:41], vcc
	s_andn2_b64 s[40:41], s[40:41], vcc
	s_and_saveexec_b64 s[32:33], s[44:45]
	v_lshlrev_b32_e32 v34, 2, v67
	ds_read_b32 v7, v34 offset:10256
	s_mov_b64 exec, s[32:33]
	s_and_saveexec_b64 s[32:33], s[40:41]
	v_add_lshl_u32 v34, v67, s46, 2
	global_load_dword v7, v34, s[12:13]
	s_mov_b64 exec, s[32:33]
	v_add_u32_e32 v68, 8, v68
	v_cmp_gt_i32_e64 s[40:41], v11, v68
	v_add_u32_e32 v67, 8, v67
	v_cmp_gt_u32_e32 vcc, 0x400, v67
	s_and_b64 s[44:45], s[40:41], vcc
	s_andn2_b64 s[40:41], s[40:41], vcc
	s_and_saveexec_b64 s[32:33], s[44:45]
	v_lshlrev_b32_e32 v35, 2, v67
	ds_read_b32 v8, v35 offset:10256
	s_mov_b64 exec, s[32:33]
	s_and_saveexec_b64 s[32:33], s[40:41]
	v_add_lshl_u32 v35, v67, s46, 2
	global_load_dword v8, v35, s[12:13]
	s_mov_b64 exec, s[32:33]
	s_waitcnt vmcnt(0) lgkmcnt(0)
	v_lshlrev_b32_e32 v5, 4, v5
	v_lshlrev_b32_e32 v6, 4, v6
	v_lshlrev_b32_e32 v7, 4, v7
	v_lshlrev_b32_e32 v8, 4, v8

	.amdhsa_kernel _Z11agg1_kernelPKDF16_PKfS2_PKiS4_S2_S2_PDF16_PfS6_i
		.amdhsa_group_segment_fixed_size 14352
		.amdhsa_private_segment_fixed_size 0
		.amdhsa_kernarg_size 84
		.amdhsa_user_sgpr_count 2
		.amdhsa_user_sgpr_dispatch_ptr 0
		.amdhsa_user_sgpr_queue_ptr 0
		.amdhsa_user_sgpr_kernarg_segment_ptr 1
		.amdhsa_user_sgpr_dispatch_id 0
		.amdhsa_user_sgpr_kernarg_preload_length 0
		.amdhsa_user_sgpr_kernarg_preload_offset 0
		.amdhsa_user_sgpr_private_segment_size 0
		.amdhsa_uses_dynamic_stack 0
		.amdhsa_enable_private_segment 0
		.amdhsa_system_sgpr_workgroup_id_x 1
		.amdhsa_system_sgpr_workgroup_id_y 0
		.amdhsa_system_sgpr_workgroup_id_z 0
		.amdhsa_system_sgpr_workgroup_info 0
		.amdhsa_system_vgpr_workitem_id 0
		.amdhsa_next_free_vgpr 70
		.amdhsa_next_free_sgpr 48
		.amdhsa_accum_offset 72
		.amdhsa_reserve_vcc 1
		.amdhsa_float_round_mode_32 0
		.amdhsa_float_round_mode_16_64 0
		.amdhsa_float_denorm_mode_32 3
		.amdhsa_float_denorm_mode_16_64 3
		.amdhsa_dx10_clamp 1
		.amdhsa_ieee_mode 1
		.amdhsa_fp16_overflow 0
		.amdhsa_tg_split 0
		.amdhsa_exception_fp_ieee_invalid_op 0
		.amdhsa_exception_fp_denorm_src 0
		.amdhsa_exception_fp_ieee_div_zero 0
		.amdhsa_exception_fp_ieee_overflow 0
		.amdhsa_exception_fp_ieee_underflow 0
		.amdhsa_exception_fp_ieee_inexact 0
		.amdhsa_exception_int_div_zero 0
	.end_amdhsa_kernel

amdhsa.kernels:
  - .agpr_count:     0
    .args:
      - .actual_access:  read_only
        .address_space:  global
        .offset:         0
        .size:           8
        .value_kind:     global_buffer
      - .actual_access:  read_only
        .address_space:  global
        .offset:         8
        .size:           8
        .value_kind:     global_buffer
      - .actual_access:  read_only
        .address_space:  global
        .offset:         16
        .size:           8
        .value_kind:     global_buffer
      - .actual_access:  read_only
        .address_space:  global
        .offset:         24
        .size:           8
        .value_kind:     global_buffer
      - .actual_access:  read_only
        .address_space:  global
        .offset:         32
        .size:           8
        .value_kind:     global_buffer
      - .actual_access:  read_only
        .address_space:  global
        .offset:         40
        .size:           8
        .value_kind:     global_buffer
      - .actual_access:  read_only
        .address_space:  global
        .offset:         48
        .size:           8
        .value_kind:     global_buffer
      - .actual_access:  read_only
        .address_space:  global
        .offset:         56
        .size:           8
        .value_kind:     global_buffer
      - .actual_access:  read_only
        .address_space:  global
        .offset:         64
        .size:           8
        .value_kind:     global_buffer
      - .actual_access:  read_only
        .address_space:  global
        .offset:         72
        .size:           8
        .value_kind:     global_buffer
      - .actual_access:  read_only
        .address_space:  global
        .offset:         80
        .size:           8
        .value_kind:     global_buffer
      - .actual_access:  read_only
        .address_space:  global
        .offset:         88
        .size:           8
        .value_kind:     global_buffer
      - .actual_access:  read_only
        .address_space:  global
        .offset:         96
        .size:           8
        .value_kind:     global_buffer
      - .actual_access:  write_only
        .address_space:  global
        .offset:         104
        .size:           8
        .value_kind:     global_buffer
      - .actual_access:  write_only
        .address_space:  global
        .offset:         112
        .size:           8
        .value_kind:     global_buffer
      - .actual_access:  write_only
        .address_space:  global
        .offset:         120
        .size:           8
        .value_kind:     global_buffer
      - .actual_access:  write_only
        .address_space:  global
        .offset:         128
        .size:           8
        .value_kind:     global_buffer
      - .actual_access:  write_only
        .address_space:  global
        .offset:         136
        .size:           8
        .value_kind:     global_buffer
      - .actual_access:  write_only
        .address_space:  global
        .offset:         144
        .size:           8
        .value_kind:     global_buffer
      - .actual_access:  write_only
        .address_space:  global
        .offset:         152
        .size:           8
        .value_kind:     global_buffer
      - .actual_access:  write_only
        .address_space:  global
        .offset:         160
        .size:           8
        .value_kind:     global_buffer
      - .actual_access:  write_only
        .address_space:  global
        .offset:         168
        .size:           8
        .value_kind:     global_buffer
      - .actual_access:  read_only
        .address_space:  global
        .offset:         176
        .size:           8
        .value_kind:     global_buffer
    .group_segment_fixed_size: 29696
    .kernarg_segment_align: 8
    .kernarg_segment_size: 184
    .language:       OpenCL C
    .language_version:
      - 2
      - 0
    .max_flat_workgroup_size: 512
    .name:           _Z12front_kernelPKiS0_PKfS2_S2_S2_S2_S2_S2_S2_S2_S2_S2_PjS3_PiS4_PDF16_PfS6_S4_S5_S0_
    .private_segment_fixed_size: 0
    .sgpr_count:     30
    .sgpr_spill_count: 0
    .symbol:         _Z12front_kernelPKiS0_PKfS2_S2_S2_S2_S2_S2_S2_S2_S2_S2_PjS3_PiS4_PDF16_PfS6_S4_S5_S0_.kd
    .uniform_work_group_size: 1
    .uses_dynamic_stack: false
    .vgpr_count:     80
    .vgpr_spill_count: 0
    .wavefront_size: 64
  - .agpr_count:     0
    .args:
      - .actual_access:  read_only
        .address_space:  global
        .offset:         0
        .size:           8
        .value_kind:     global_buffer
      - .actual_access:  read_only
        .address_space:  global
        .offset:         8
        .size:           8
        .value_kind:     global_buffer
      - .actual_access:  write_only
        .address_space:  global
        .offset:         16
        .size:           8
        .value_kind:     global_buffer
      - .actual_access:  write_only
        .address_space:  global
        .offset:         24
        .size:           8
        .value_kind:     global_buffer
      - .actual_access:  write_only
        .address_space:  global
        .offset:         32
        .size:           8
        .value_kind:     global_buffer
      - .actual_access:  read_only
        .address_space:  global
        .offset:         40
        .size:           8
        .value_kind:     global_buffer
      - .actual_access:  read_only
        .address_space:  global
        .offset:         48
        .size:           8
        .value_kind:     global_buffer
      - .actual_access:  write_only
        .address_space:  global
        .offset:         56
        .size:           8
        .value_kind:     global_buffer
      - .actual_access:  write_only
        .address_space:  global
        .offset:         64
        .size:           8
        .value_kind:     global_buffer
    .group_segment_fixed_size: 40960
    .kernarg_segment_align: 8
    .kernarg_segment_size: 72
    .language:       OpenCL C
    .language_version:
      - 2
      - 0
    .max_flat_workgroup_size: 512
    .name:           _Z13second_kernelPKfPKDF16_PDF16_PfS4_PKjPKiPiS9_
    .private_segment_fixed_size: 0
    .sgpr_count:     29
    .sgpr_spill_count: 0
    .symbol:         _Z13second_kernelPKfPKDF16_PDF16_PfS4_PKjPKiPiS9_.kd
    .uniform_work_group_size: 1
    .uses_dynamic_stack: false
    .vgpr_count:     64
    .vgpr_spill_count: 0
    .wavefront_size: 64
  - .agpr_count:     0
    .args:
      - .actual_access:  read_only
        .address_space:  global
        .offset:         0
        .size:           8
        .value_kind:     global_buffer
      - .actual_access:  read_only
        .address_space:  global
        .offset:         8
        .size:           8
        .value_kind:     global_buffer
      - .actual_access:  read_only
        .address_space:  global
        .offset:         16
        .size:           8
        .value_kind:     global_buffer
      - .actual_access:  read_only
        .address_space:  global
        .offset:         24
        .size:           8
        .value_kind:     global_buffer
      - .actual_access:  read_only
        .address_space:  global
        .offset:         32
        .size:           8
        .value_kind:     global_buffer
      - .actual_access:  read_only
        .address_space:  global
        .offset:         40
        .size:           8
        .value_kind:     global_buffer
      - .actual_access:  read_only
        .address_space:  global
        .offset:         48
        .size:           8
        .value_kind:     global_buffer
      - .actual_access:  write_only
        .address_space:  global
        .offset:         56
        .size:           8
        .value_kind:     global_buffer
      - .actual_access:  write_only
        .address_space:  global
        .offset:         64
        .size:           8
        .value_kind:     global_buffer
      - .actual_access:  write_only
        .address_space:  global
        .offset:         72
        .size:           8
        .value_kind:     global_buffer
      - .offset:         80
        .size:           4
        .value_kind:     by_value
    .group_segment_fixed_size: 14352
    .kernarg_segment_align: 8
    .kernarg_segment_size: 84
    .language:       OpenCL C
    .language_version:
      - 2
      - 0
    .max_flat_workgroup_size: 256
    .name:           _Z11agg1_kernelPKDF16_PKfS2_PKiS4_S2_S2_PDF16_PfS6_i
    .private_segment_fixed_size: 0
    .sgpr_count:     54
    .sgpr_spill_count: 0
    .symbol:         _Z11agg1_kernelPKDF16_PKfS2_PKiS4_S2_S2_PDF16_PfS6_i.kd
    .uniform_work_group_size: 1
    .uses_dynamic_stack: false
    .vgpr_count:     70
    .vgpr_spill_count: 0
    .wavefront_size: 64
  - .agpr_count:     0
    .args:
      - .actual_access:  read_only
        .address_space:  global
        .offset:         0
        .size:           8
        .value_kind:     global_buffer
      - .actual_access:  read_only
        .address_space:  global
        .offset:         8
        .size:           8
        .value_kind:     global_buffer
      - .actual_access:  read_only
        .address_space:  global
        .offset:         16
        .size:           8
        .value_kind:     global_buffer
      - .actual_access:  read_only
        .address_space:  global
        .offset:         24
        .size:           8
        .value_kind:     global_buffer
      - .actual_access:  read_only
        .address_space:  global
        .offset:         32
        .size:           8
        .value_kind:     global_buffer
      - .actual_access:  write_only
        .address_space:  global
        .offset:         40
        .size:           8
        .value_kind:     global_buffer
      - .offset:         48
        .size:           4
        .value_kind:     by_value
    .group_segment_fixed_size: 0
    .kernarg_segment_align: 8
    .kernarg_segment_size: 52
    .language:       OpenCL C
    .language_version:
      - 2
      - 0
    .max_flat_workgroup_size: 256
    .name:           _Z13stats2_kernelPKiS0_PKfS2_S0_P15HIP_vector_typeIfLj4EEi
    .private_segment_fixed_size: 0
    .sgpr_count:     27
    .sgpr_spill_count: 0
    .symbol:         _Z13stats2_kernelPKiS0_PKfS2_S0_P15HIP_vector_typeIfLj4EEi.kd
    .uniform_work_group_size: 1
    .uses_dynamic_stack: false
    .vgpr_count:     32
    .vgpr_spill_count: 0
    .wavefront_size: 64
  - .agpr_count:     0
    .args:
      - .actual_access:  read_only
        .address_space:  global
        .offset:         0
        .size:           8
        .value_kind:     global_buffer
      - .actual_access:  read_only
        .address_space:  global
        .offset:         8
        .size:           8
        .value_kind:     global_buffer
      - .actual_access:  read_only
        .address_space:  global
        .offset:         16
        .size:           8
        .value_kind:     global_buffer
      - .actual_access:  read_only
        .address_space:  global
        .offset:         24
        .size:           8
        .value_kind:     global_buffer
      - .actual_access:  read_only
        .address_space:  global
        .offset:         32
        .size:           8
        .value_kind:     global_buffer
      - .actual_access:  write_only
        .address_space:  global
        .offset:         40
        .size:           8
        .value_kind:     global_buffer
      - .offset:         48
        .size:           4
        .value_kind:     by_value
    .group_segment_fixed_size: 70752
    .kernarg_segment_align: 8
    .kernarg_segment_size: 52
    .language:       OpenCL C
    .language_version:
      - 2
      - 0
    .max_flat_workgroup_size: 1024
    .name:           _Z12pool2_kernelPKjPKiPKfPK15HIP_vector_typeIfLj4EEPKDF16_Pfi
    .private_segment_fixed_size: 0
    .sgpr_count:     26
    .sgpr_spill_count: 0
    .symbol:         _Z12pool2_kernelPKjPKiPKfPK15HIP_vector_typeIfLj4EEPKDF16_Pfi.kd
    .uniform_work_group_size: 1
    .uses_dynamic_stack: false
    .vgpr_count:     128
    .vgpr_spill_count: 0
    .wavefront_size: 64
  - .agpr_count:     0
    .args:
      - .actual_access:  read_only
        .address_space:  global
        .offset:         0
        .size:           8
        .value_kind:     global_buffer
      - .actual_access:  read_only
        .address_space:  global
        .offset:         8
        .size:           8
        .value_kind:     global_buffer
      - .actual_access:  read_only
        .address_space:  global
        .offset:         16
        .size:           8
        .value_kind:     global_buffer
      - .actual_access:  read_only
        .address_space:  global
        .offset:         24
        .size:           8
        .value_kind:     global_buffer
      - .actual_access:  read_only
        .address_space:  global
        .offset:         32
        .size:           8
        .value_kind:     global_buffer
      - .actual_access:  read_only
        .address_space:  global
        .offset:         40
        .size:           8
        .value_kind:     global_buffer
      - .actual_access:  read_only
        .address_space:  global
        .offset:         48
        .size:           8
        .value_kind:     global_buffer
      - .actual_access:  read_only
        .address_space:  global
        .offset:         56
        .size:           8
        .value_kind:     global_buffer
      - .actual_access:  write_only
        .address_space:  global
        .offset:         64
        .size:           8
        .value_kind:     global_buffer
    .group_segment_fixed_size: 9472
    .kernarg_segment_align: 8
    .kernarg_segment_size: 72
    .language:       OpenCL C
    .language_version:
      - 2
      - 0
    .max_flat_workgroup_size: 1024
    .name:           _Z10mlp_kernelPKfPKiS0_S0_S0_S0_S0_S0_Pf
    .private_segment_fixed_size: 0
    .sgpr_count:     76
    .sgpr_spill_count: 0
    .symbol:         _Z10mlp_kernelPKfPKiS0_S0_S0_S0_S0_S0_Pf.kd
    .uniform_work_group_size: 1
    .uses_dynamic_stack: false
    .vgpr_count:     77
    .vgpr_spill_count: 0
    .wavefront_size: 64
